# gemm: MFMA-first restart - LDS-DMA slots moved from 0,6,12 to 1,7,13 in both blocks so the first MFMA issues right after each wait/barrier (on top of the balanced read split)
# speedup vs baseline: 1.0009x; 1.0009x over previous
.Lgemm_T_loop:
	s_waitcnt lgkmcnt(0)
	ds_read_b128 v[146:149], v164
	v_mfma_f32_16x16x32_f16 v[82:85], v[134:137], v[86:89], v[82:85]
	s_add_u32 m0, s11, 0x1e080
	ds_read_b128 v[150:153], v164 offset:2048
	global_load_lds_dwordx4 v[220:221], off offset:-128
	v_mfma_f32_16x16x32_f16 v[58:61], v[138:141], v[86:89], v[58:61]
	ds_read_b128 v[154:157], v164 offset:4096
	v_mfma_f32_16x16x32_f16 v[14:17], v[142:145], v[86:89], v[14:17]
	ds_read_b128 v[110:113], v160
	v_mfma_f32_16x16x32_f16 v[78:81], v[134:137], v[90:93], v[78:81]
	ds_read_b128 v[114:117], v160 offset:2048
	v_mfma_f32_16x16x32_f16 v[22:25], v[138:141], v[90:93], v[22:25]
	ds_read_b128 v[118:121], v160 offset:4096
	v_mfma_f32_16x16x32_f16 v[30:33], v[142:145], v[90:93], v[30:33]
	ds_read_b128 v[122:125], v160 offset:6144
	v_mfma_f32_16x16x32_f16 v[74:77], v[134:137], v[94:97], v[74:77]
	s_add_u32 m0, s11, 0x20080
	ds_read_b128 v[126:129], v160 offset:8192
	global_load_lds_dwordx4 v[224:225], off offset:-128
	v_mfma_f32_16x16x32_f16 v[18:21], v[138:141], v[94:97], v[18:21]
	ds_read_b128 v[130:133], v160 offset:10240
	v_mfma_f32_16x16x32_f16 v[26:29], v[142:145], v[94:97], v[26:29]
	v_mfma_f32_16x16x32_f16 v[70:73], v[134:137], v[98:101], v[70:73]
	v_mfma_f32_16x16x32_f16 v[46:49], v[138:141], v[98:101], v[46:49]
	v_mfma_f32_16x16x32_f16 v[240:243], v[142:145], v[98:101], v[240:243]
	v_mfma_f32_16x16x32_f16 v[66:69], v[134:137], v[102:105], v[66:69]
	s_add_u32 m0, s11, 0x22080
	v_mfma_f32_16x16x32_f16 v[42:45], v[138:141], v[102:105], v[42:45]
	global_load_lds_dwordx4 v[228:229], off offset:-128
	v_mfma_f32_16x16x32_f16 v[236:239], v[142:145], v[102:105], v[236:239]
	v_mfma_f32_16x16x32_f16 v[62:65], v[134:137], v[106:109], v[62:65]
	v_mfma_f32_16x16x32_f16 v[38:41], v[138:141], v[106:109], v[38:41]
	v_mfma_f32_16x16x32_f16 v[34:37], v[142:145], v[106:109], v[34:37]
	s_waitcnt vmcnt(6) lgkmcnt(0)
	s_barrier
	ds_read_b128 v[134:137], v162 offset:49152
	v_mfma_f32_16x16x32_f16 v[82:85], v[146:149], v[110:113], v[82:85]
	s_add_u32 m0, s11, 0x0
	ds_read_b128 v[138:141], v162 offset:51200
	global_load_lds_dwordx4 v[218:219], off
	v_mfma_f32_16x16x32_f16 v[58:61], v[150:153], v[110:113], v[58:61]
	ds_read_b128 v[142:145], v162 offset:53248
	v_mfma_f32_16x16x32_f16 v[14:17], v[154:157], v[110:113], v[14:17]
	ds_read_b128 v[86:89], v158 offset:49152
	v_mfma_f32_16x16x32_f16 v[78:81], v[146:149], v[114:117], v[78:81]
	ds_read_b128 v[90:93], v158 offset:51200
	v_mfma_f32_16x16x32_f16 v[22:25], v[150:153], v[114:117], v[22:25]
	ds_read_b128 v[94:97], v158 offset:53248
	v_mfma_f32_16x16x32_f16 v[30:33], v[154:157], v[114:117], v[30:33]
	ds_read_b128 v[98:101], v158 offset:55296
	v_mfma_f32_16x16x32_f16 v[74:77], v[146:149], v[118:121], v[74:77]
	s_add_u32 m0, s11, 0x2000
	ds_read_b128 v[102:105], v158 offset:57344
	global_load_lds_dwordx4 v[222:223], off
	v_mfma_f32_16x16x32_f16 v[18:21], v[150:153], v[118:121], v[18:21]
	ds_read_b128 v[106:109], v158 offset:59392
	v_mfma_f32_16x16x32_f16 v[26:29], v[154:157], v[118:121], v[26:29]
	v_mfma_f32_16x16x32_f16 v[70:73], v[146:149], v[122:125], v[70:73]
	v_mfma_f32_16x16x32_f16 v[46:49], v[150:153], v[122:125], v[46:49]
	v_mfma_f32_16x16x32_f16 v[240:243], v[154:157], v[122:125], v[240:243]
	v_mfma_f32_16x16x32_f16 v[66:69], v[146:149], v[126:129], v[66:69]
	s_add_u32 m0, s11, 0x4000
	v_mfma_f32_16x16x32_f16 v[42:45], v[150:153], v[126:129], v[42:45]
	global_load_lds_dwordx4 v[226:227], off
	v_mfma_f32_16x16x32_f16 v[236:239], v[154:157], v[126:129], v[236:239]
	v_mfma_f32_16x16x32_f16 v[62:65], v[146:149], v[130:133], v[62:65]
	v_mfma_f32_16x16x32_f16 v[38:41], v[150:153], v[130:133], v[38:41]
	v_mfma_f32_16x16x32_f16 v[34:37], v[154:157], v[130:133], v[34:37]
	s_waitcnt lgkmcnt(0)
	ds_read_b128 v[146:149], v164 offset:49152
	v_mfma_f32_16x16x32_f16 v[82:85], v[134:137], v[86:89], v[82:85]
	s_add_u32 m0, s11, 0x6000
	ds_read_b128 v[150:153], v164 offset:51200
	global_load_lds_dwordx4 v[220:221], off
	v_mfma_f32_16x16x32_f16 v[58:61], v[138:141], v[86:89], v[58:61]
	ds_read_b128 v[154:157], v164 offset:53248
	v_mfma_f32_16x16x32_f16 v[14:17], v[142:145], v[86:89], v[14:17]
	ds_read_b128 v[110:113], v160 offset:49152
	v_mfma_f32_16x16x32_f16 v[78:81], v[134:137], v[90:93], v[78:81]
	ds_read_b128 v[114:117], v160 offset:51200
	v_mfma_f32_16x16x32_f16 v[22:25], v[138:141], v[90:93], v[22:25]
	ds_read_b128 v[118:121], v160 offset:53248
	v_mfma_f32_16x16x32_f16 v[30:33], v[142:145], v[90:93], v[30:33]
	ds_read_b128 v[122:125], v160 offset:55296
	v_mfma_f32_16x16x32_f16 v[74:77], v[134:137], v[94:97], v[74:77]
	s_add_u32 m0, s11, 0x8000
	ds_read_b128 v[126:129], v160 offset:57344
	global_load_lds_dwordx4 v[224:225], off
	v_mfma_f32_16x16x32_f16 v[18:21], v[138:141], v[94:97], v[18:21]
	ds_read_b128 v[130:133], v160 offset:59392
	v_mfma_f32_16x16x32_f16 v[26:29], v[142:145], v[94:97], v[26:29]
	v_mfma_f32_16x16x32_f16 v[70:73], v[134:137], v[98:101], v[70:73]
	v_mfma_f32_16x16x32_f16 v[46:49], v[138:141], v[98:101], v[46:49]
	v_mfma_f32_16x16x32_f16 v[240:243], v[142:145], v[98:101], v[240:243]
	v_mfma_f32_16x16x32_f16 v[66:69], v[134:137], v[102:105], v[66:69]
	s_add_u32 m0, s11, 0xa000
	v_mfma_f32_16x16x32_f16 v[42:45], v[138:141], v[102:105], v[42:45]
	global_load_lds_dwordx4 v[228:229], off
	v_mfma_f32_16x16x32_f16 v[236:239], v[142:145], v[102:105], v[236:239]
	v_mfma_f32_16x16x32_f16 v[62:65], v[134:137], v[106:109], v[62:65]
	v_mfma_f32_16x16x32_f16 v[38:41], v[138:141], v[106:109], v[38:41]
	v_mfma_f32_16x16x32_f16 v[34:37], v[142:145], v[106:109], v[34:37]
	s_waitcnt vmcnt(6) lgkmcnt(0)
	s_barrier
	ds_read_b128 v[134:137], v163
	v_mfma_f32_16x16x32_f16 v[82:85], v[146:149], v[110:113], v[82:85]
	s_add_u32 m0, s11, 0xbf80
	ds_read_b128 v[138:141], v163 offset:2048
	global_load_lds_dwordx4 v[218:219], off offset:128
	v_mfma_f32_16x16x32_f16 v[58:61], v[150:153], v[110:113], v[58:61]
	ds_read_b128 v[142:145], v163 offset:4096
	v_mfma_f32_16x16x32_f16 v[14:17], v[154:157], v[110:113], v[14:17]
	ds_read_b128 v[86:89], v159
	v_mfma_f32_16x16x32_f16 v[78:81], v[146:149], v[114:117], v[78:81]
	ds_read_b128 v[90:93], v159 offset:2048
	v_mfma_f32_16x16x32_f16 v[22:25], v[150:153], v[114:117], v[22:25]
	ds_read_b128 v[94:97], v159 offset:4096
	v_mfma_f32_16x16x32_f16 v[30:33], v[154:157], v[114:117], v[30:33]
	ds_read_b128 v[98:101], v159 offset:6144
	v_mfma_f32_16x16x32_f16 v[74:77], v[146:149], v[118:121], v[74:77]
	s_add_u32 m0, s11, 0xdf80
	ds_read_b128 v[102:105], v159 offset:8192
	global_load_lds_dwordx4 v[222:223], off offset:128
	v_mfma_f32_16x16x32_f16 v[18:21], v[150:153], v[118:121], v[18:21]
	ds_read_b128 v[106:109], v159 offset:10240
	v_mfma_f32_16x16x32_f16 v[26:29], v[154:157], v[118:121], v[26:29]
	v_mfma_f32_16x16x32_f16 v[70:73], v[146:149], v[122:125], v[70:73]
	v_mfma_f32_16x16x32_f16 v[46:49], v[150:153], v[122:125], v[46:49]
	v_mfma_f32_16x16x32_f16 v[240:243], v[154:157], v[122:125], v[240:243]
	v_mfma_f32_16x16x32_f16 v[66:69], v[146:149], v[126:129], v[66:69]
	s_add_u32 m0, s11, 0xff80
	v_mfma_f32_16x16x32_f16 v[42:45], v[150:153], v[126:129], v[42:45]
	global_load_lds_dwordx4 v[226:227], off offset:128
	v_mfma_f32_16x16x32_f16 v[236:239], v[154:157], v[126:129], v[236:239]
	v_mfma_f32_16x16x32_f16 v[62:65], v[146:149], v[130:133], v[62:65]
	v_mfma_f32_16x16x32_f16 v[38:41], v[150:153], v[130:133], v[38:41]
	v_mfma_f32_16x16x32_f16 v[34:37], v[154:157], v[130:133], v[34:37]
	s_waitcnt lgkmcnt(0)
	ds_read_b128 v[146:149], v165
	v_mfma_f32_16x16x32_f16 v[82:85], v[134:137], v[86:89], v[82:85]
	s_add_u32 m0, s11, 0x11f80
	ds_read_b128 v[150:153], v165 offset:2048
	global_load_lds_dwordx4 v[220:221], off offset:128
	v_mfma_f32_16x16x32_f16 v[58:61], v[138:141], v[86:89], v[58:61]
	ds_read_b128 v[154:157], v165 offset:4096
	v_mfma_f32_16x16x32_f16 v[14:17], v[142:145], v[86:89], v[14:17]
	ds_read_b128 v[110:113], v161
	v_mfma_f32_16x16x32_f16 v[78:81], v[134:137], v[90:93], v[78:81]
	ds_read_b128 v[114:117], v161 offset:2048
	v_mfma_f32_16x16x32_f16 v[22:25], v[138:141], v[90:93], v[22:25]
	ds_read_b128 v[118:121], v161 offset:4096
	v_mfma_f32_16x16x32_f16 v[30:33], v[142:145], v[90:93], v[30:33]
	ds_read_b128 v[122:125], v161 offset:6144
	v_mfma_f32_16x16x32_f16 v[74:77], v[134:137], v[94:97], v[74:77]
	s_add_u32 m0, s11, 0x13f80
	ds_read_b128 v[126:129], v161 offset:8192
	global_load_lds_dwordx4 v[224:225], off offset:128
	v_mfma_f32_16x16x32_f16 v[18:21], v[138:141], v[94:97], v[18:21]
	ds_read_b128 v[130:133], v161 offset:10240
	v_mfma_f32_16x16x32_f16 v[26:29], v[142:145], v[94:97], v[26:29]
	v_mfma_f32_16x16x32_f16 v[70:73], v[134:137], v[98:101], v[70:73]
	v_mfma_f32_16x16x32_f16 v[46:49], v[138:141], v[98:101], v[46:49]
	v_mfma_f32_16x16x32_f16 v[240:243], v[142:145], v[98:101], v[240:243]
	v_mfma_f32_16x16x32_f16 v[66:69], v[134:137], v[102:105], v[66:69]
	s_add_u32 m0, s11, 0x15f80
	v_mfma_f32_16x16x32_f16 v[42:45], v[138:141], v[102:105], v[42:45]
	global_load_lds_dwordx4 v[228:229], off offset:128
	v_mfma_f32_16x16x32_f16 v[236:239], v[142:145], v[102:105], v[236:239]
	v_mfma_f32_16x16x32_f16 v[62:65], v[134:137], v[106:109], v[62:65]
	v_mfma_f32_16x16x32_f16 v[38:41], v[138:141], v[106:109], v[38:41]
	v_mfma_f32_16x16x32_f16 v[34:37], v[142:145], v[106:109], v[34:37]
	s_waitcnt vmcnt(6) lgkmcnt(0)
	s_barrier
	ds_read_b128 v[134:137], v162
	v_mfma_f32_16x16x32_f16 v[82:85], v[146:149], v[110:113], v[82:85]
	s_add_u32 m0, s11, 0x17f00
	ds_read_b128 v[138:141], v162 offset:2048
	global_load_lds_dwordx4 v[218:219], off offset:256
	v_mfma_f32_16x16x32_f16 v[58:61], v[150:153], v[110:113], v[58:61]
	ds_read_b128 v[142:145], v162 offset:4096
	v_mfma_f32_16x16x32_f16 v[14:17], v[154:157], v[110:113], v[14:17]
	ds_read_b128 v[86:89], v158
	v_mfma_f32_16x16x32_f16 v[78:81], v[146:149], v[114:117], v[78:81]
	ds_read_b128 v[90:93], v158 offset:2048
	v_mfma_f32_16x16x32_f16 v[22:25], v[150:153], v[114:117], v[22:25]
	ds_read_b128 v[94:97], v158 offset:4096
	v_mfma_f32_16x16x32_f16 v[30:33], v[154:157], v[114:117], v[30:33]
	ds_read_b128 v[98:101], v158 offset:6144
	v_mfma_f32_16x16x32_f16 v[74:77], v[146:149], v[118:121], v[74:77]
	s_add_u32 m0, s11, 0x19f00
	ds_read_b128 v[102:105], v158 offset:8192
	global_load_lds_dwordx4 v[222:223], off offset:256
	v_mfma_f32_16x16x32_f16 v[18:21], v[150:153], v[118:121], v[18:21]
	ds_read_b128 v[106:109], v158 offset:10240
	v_mfma_f32_16x16x32_f16 v[26:29], v[154:157], v[118:121], v[26:29]
	v_mfma_f32_16x16x32_f16 v[70:73], v[146:149], v[122:125], v[70:73]
	v_mfma_f32_16x16x32_f16 v[46:49], v[150:153], v[122:125], v[46:49]
	v_mfma_f32_16x16x32_f16 v[240:243], v[154:157], v[122:125], v[240:243]
	v_mfma_f32_16x16x32_f16 v[66:69], v[146:149], v[126:129], v[66:69]
	s_add_u32 m0, s11, 0x1bf00
	v_mfma_f32_16x16x32_f16 v[42:45], v[150:153], v[126:129], v[42:45]
	global_load_lds_dwordx4 v[226:227], off offset:256
	v_mfma_f32_16x16x32_f16 v[236:239], v[154:157], v[126:129], v[236:239]
	v_mfma_f32_16x16x32_f16 v[62:65], v[146:149], v[130:133], v[62:65]
	v_mfma_f32_16x16x32_f16 v[38:41], v[150:153], v[130:133], v[38:41]
	v_mfma_f32_16x16x32_f16 v[34:37], v[154:157], v[130:133], v[34:37]
	v_lshl_add_u64 v[218:219], v[218:219], 0, s[20:21]
	v_lshl_add_u64 v[222:223], v[222:223], 0, s[20:21]
	v_lshl_add_u64 v[226:227], v[226:227], 0, s[20:21]
	v_lshl_add_u64 v[220:221], v[220:221], 0, s[20:21]
	v_lshl_add_u64 v[224:225], v[224:225], 0, s[20:21]
	v_lshl_add_u64 v[228:229], v[228:229], 0, s[20:21]
	s_sub_u32 s22, s22, 1
	s_cmp_lg_u32 s22, 0
	s_cbranch_scc1 .Lgemm_T_loop
	s_waitcnt lgkmcnt(0)
	ds_read_b128 v[146:149], v164
	v_mfma_f32_16x16x32_f16 v[82:85], v[134:137], v[86:89], v[82:85]
	s_add_u32 m0, s11, 0x1e080
	ds_read_b128 v[150:153], v164 offset:2048
	global_load_lds_dwordx4 v[220:221], off offset:-128
	v_mfma_f32_16x16x32_f16 v[58:61], v[138:141], v[86:89], v[58:61]
	ds_read_b128 v[154:157], v164 offset:4096
	v_mfma_f32_16x16x32_f16 v[14:17], v[142:145], v[86:89], v[14:17]
	ds_read_b128 v[110:113], v160
	v_mfma_f32_16x16x32_f16 v[78:81], v[134:137], v[90:93], v[78:81]
	ds_read_b128 v[114:117], v160 offset:2048
	v_mfma_f32_16x16x32_f16 v[22:25], v[138:141], v[90:93], v[22:25]
	ds_read_b128 v[118:121], v160 offset:4096
	v_mfma_f32_16x16x32_f16 v[30:33], v[142:145], v[90:93], v[30:33]
	ds_read_b128 v[122:125], v160 offset:6144
	v_mfma_f32_16x16x32_f16 v[74:77], v[134:137], v[94:97], v[74:77]
	s_add_u32 m0, s11, 0x20080
	ds_read_b128 v[126:129], v160 offset:8192
	global_load_lds_dwordx4 v[224:225], off offset:-128
	v_mfma_f32_16x16x32_f16 v[18:21], v[138:141], v[94:97], v[18:21]
	ds_read_b128 v[130:133], v160 offset:10240
	v_mfma_f32_16x16x32_f16 v[26:29], v[142:145], v[94:97], v[26:29]
	v_mfma_f32_16x16x32_f16 v[70:73], v[134:137], v[98:101], v[70:73]
	v_mfma_f32_16x16x32_f16 v[46:49], v[138:141], v[98:101], v[46:49]
	v_mfma_f32_16x16x32_f16 v[240:243], v[142:145], v[98:101], v[240:243]
	v_mfma_f32_16x16x32_f16 v[66:69], v[134:137], v[102:105], v[66:69]
	s_add_u32 m0, s11, 0x22080
	v_mfma_f32_16x16x32_f16 v[42:45], v[138:141], v[102:105], v[42:45]
	global_load_lds_dwordx4 v[228:229], off offset:-128
	v_mfma_f32_16x16x32_f16 v[236:239], v[142:145], v[102:105], v[236:239]
	v_mfma_f32_16x16x32_f16 v[62:65], v[134:137], v[106:109], v[62:65]
	v_mfma_f32_16x16x32_f16 v[38:41], v[138:141], v[106:109], v[38:41]
	v_mfma_f32_16x16x32_f16 v[34:37], v[142:145], v[106:109], v[34:37]
	s_waitcnt vmcnt(6) lgkmcnt(0)
	s_barrier
	ds_read_b128 v[134:137], v162 offset:49152
	v_mfma_f32_16x16x32_f16 v[82:85], v[146:149], v[110:113], v[82:85]
	s_add_u32 m0, s11, 0x0
	ds_read_b128 v[138:141], v162 offset:51200
	global_load_lds_dwordx4 v[218:219], off
	v_mfma_f32_16x16x32_f16 v[58:61], v[150:153], v[110:113], v[58:61]
	ds_read_b128 v[142:145], v162 offset:53248
	v_mfma_f32_16x16x32_f16 v[14:17], v[154:157], v[110:113], v[14:17]
	ds_read_b128 v[86:89], v158 offset:49152
	v_mfma_f32_16x16x32_f16 v[78:81], v[146:149], v[114:117], v[78:81]
	ds_read_b128 v[90:93], v158 offset:51200
	v_mfma_f32_16x16x32_f16 v[22:25], v[150:153], v[114:117], v[22:25]
	ds_read_b128 v[94:97], v158 offset:53248
	v_mfma_f32_16x16x32_f16 v[30:33], v[154:157], v[114:117], v[30:33]
	ds_read_b128 v[98:101], v158 offset:55296
	v_mfma_f32_16x16x32_f16 v[74:77], v[146:149], v[118:121], v[74:77]
	s_add_u32 m0, s11, 0x2000
	ds_read_b128 v[102:105], v158 offset:57344
	global_load_lds_dwordx4 v[222:223], off
	v_mfma_f32_16x16x32_f16 v[18:21], v[150:153], v[118:121], v[18:21]
	ds_read_b128 v[106:109], v158 offset:59392
	v_mfma_f32_16x16x32_f16 v[26:29], v[154:157], v[118:121], v[26:29]
	v_mfma_f32_16x16x32_f16 v[70:73], v[146:149], v[122:125], v[70:73]
	v_mfma_f32_16x16x32_f16 v[46:49], v[150:153], v[122:125], v[46:49]
	v_mfma_f32_16x16x32_f16 v[240:243], v[154:157], v[122:125], v[240:243]
	v_mfma_f32_16x16x32_f16 v[66:69], v[146:149], v[126:129], v[66:69]
	s_add_u32 m0, s11, 0x4000
	v_mfma_f32_16x16x32_f16 v[42:45], v[150:153], v[126:129], v[42:45]
	global_load_lds_dwordx4 v[226:227], off
	v_mfma_f32_16x16x32_f16 v[236:239], v[154:157], v[126:129], v[236:239]
	v_mfma_f32_16x16x32_f16 v[62:65], v[146:149], v[130:133], v[62:65]
	v_mfma_f32_16x16x32_f16 v[38:41], v[150:153], v[130:133], v[38:41]
	v_mfma_f32_16x16x32_f16 v[34:37], v[154:157], v[130:133], v[34:37]
	s_waitcnt lgkmcnt(0)
	ds_read_b128 v[146:149], v164 offset:49152
	v_mfma_f32_16x16x32_f16 v[82:85], v[134:137], v[86:89], v[82:85]
	s_add_u32 m0, s11, 0x6000
	ds_read_b128 v[150:153], v164 offset:51200
	global_load_lds_dwordx4 v[220:221], off
	v_mfma_f32_16x16x32_f16 v[58:61], v[138:141], v[86:89], v[58:61]
	ds_read_b128 v[154:157], v164 offset:53248
	v_mfma_f32_16x16x32_f16 v[14:17], v[142:145], v[86:89], v[14:17]
	ds_read_b128 v[110:113], v160 offset:49152
	v_mfma_f32_16x16x32_f16 v[78:81], v[134:137], v[90:93], v[78:81]
	ds_read_b128 v[114:117], v160 offset:51200
	v_mfma_f32_16x16x32_f16 v[22:25], v[138:141], v[90:93], v[22:25]
	ds_read_b128 v[118:121], v160 offset:53248
	v_mfma_f32_16x16x32_f16 v[30:33], v[142:145], v[90:93], v[30:33]
	ds_read_b128 v[122:125], v160 offset:55296
	v_mfma_f32_16x16x32_f16 v[74:77], v[134:137], v[94:97], v[74:77]
	s_add_u32 m0, s11, 0x8000
	ds_read_b128 v[126:129], v160 offset:57344
	global_load_lds_dwordx4 v[224:225], off
	v_mfma_f32_16x16x32_f16 v[18:21], v[138:141], v[94:97], v[18:21]
	ds_read_b128 v[130:133], v160 offset:59392
	v_mfma_f32_16x16x32_f16 v[26:29], v[142:145], v[94:97], v[26:29]
	v_mfma_f32_16x16x32_f16 v[70:73], v[134:137], v[98:101], v[70:73]
	v_mfma_f32_16x16x32_f16 v[46:49], v[138:141], v[98:101], v[46:49]
	v_mfma_f32_16x16x32_f16 v[240:243], v[142:145], v[98:101], v[240:243]
	v_mfma_f32_16x16x32_f16 v[66:69], v[134:137], v[102:105], v[66:69]
	s_add_u32 m0, s11, 0xa000
	v_mfma_f32_16x16x32_f16 v[42:45], v[138:141], v[102:105], v[42:45]
	global_load_lds_dwordx4 v[228:229], off
	v_mfma_f32_16x16x32_f16 v[236:239], v[142:145], v[102:105], v[236:239]
	v_mfma_f32_16x16x32_f16 v[62:65], v[134:137], v[106:109], v[62:65]
	v_mfma_f32_16x16x32_f16 v[38:41], v[138:141], v[106:109], v[38:41]
	v_mfma_f32_16x16x32_f16 v[34:37], v[142:145], v[106:109], v[34:37]
	s_waitcnt vmcnt(6) lgkmcnt(0)
	s_barrier
	s_lshl_b32 s26, s17, 2
	s_add_u32 s26, s24, s26
	s_addc_u32 s27, s25, 0
	v_lshlrev_b32_e32 v50, 4, v231
	global_load_dwordx4 v[10:13], v50, s[26:27]
	global_load_dwordx4 v[6:9], v50, s[26:27] offset:64
	global_load_dwordx4 v[2:5], v50, s[26:27] offset:128
	ds_read_b128 v[134:137], v163
	v_mfma_f32_16x16x32_f16 v[82:85], v[146:149], v[110:113], v[82:85]
	ds_read_b128 v[138:141], v163 offset:2048
	v_mfma_f32_16x16x32_f16 v[58:61], v[150:153], v[110:113], v[58:61]
	ds_read_b128 v[142:145], v163 offset:4096
	v_mfma_f32_16x16x32_f16 v[14:17], v[154:157], v[110:113], v[14:17]
	ds_read_b128 v[86:89], v159
	v_mfma_f32_16x16x32_f16 v[78:81], v[146:149], v[114:117], v[78:81]
	ds_read_b128 v[90:93], v159 offset:2048
	v_mfma_f32_16x16x32_f16 v[22:25], v[150:153], v[114:117], v[22:25]
	ds_read_b128 v[94:97], v159 offset:4096
	v_mfma_f32_16x16x32_f16 v[30:33], v[154:157], v[114:117], v[30:33]
	ds_read_b128 v[98:101], v159 offset:6144
	v_mfma_f32_16x16x32_f16 v[74:77], v[146:149], v[118:121], v[74:77]
	ds_read_b128 v[102:105], v159 offset:8192
	v_mfma_f32_16x16x32_f16 v[18:21], v[150:153], v[118:121], v[18:21]
	ds_read_b128 v[106:109], v159 offset:10240
	v_mfma_f32_16x16x32_f16 v[26:29], v[154:157], v[118:121], v[26:29]
	v_mfma_f32_16x16x32_f16 v[70:73], v[146:149], v[122:125], v[70:73]
	v_mfma_f32_16x16x32_f16 v[46:49], v[150:153], v[122:125], v[46:49]
	v_mfma_f32_16x16x32_f16 v[240:243], v[154:157], v[122:125], v[240:243]
	v_mfma_f32_16x16x32_f16 v[66:69], v[146:149], v[126:129], v[66:69]
	v_mfma_f32_16x16x32_f16 v[42:45], v[150:153], v[126:129], v[42:45]
	v_mfma_f32_16x16x32_f16 v[236:239], v[154:157], v[126:129], v[236:239]
	v_mfma_f32_16x16x32_f16 v[62:65], v[146:149], v[130:133], v[62:65]
	v_mfma_f32_16x16x32_f16 v[38:41], v[150:153], v[130:133], v[38:41]
	v_mfma_f32_16x16x32_f16 v[34:37], v[154:157], v[130:133], v[34:37]
	s_waitcnt lgkmcnt(0)
	ds_read_b128 v[146:149], v165
	v_mfma_f32_16x16x32_f16 v[82:85], v[134:137], v[86:89], v[82:85]
	ds_read_b128 v[150:153], v165 offset:2048
	v_mfma_f32_16x16x32_f16 v[58:61], v[138:141], v[86:89], v[58:61]
	ds_read_b128 v[154:157], v165 offset:4096
	v_mfma_f32_16x16x32_f16 v[14:17], v[142:145], v[86:89], v[14:17]
	ds_read_b128 v[110:113], v161
	v_mfma_f32_16x16x32_f16 v[78:81], v[134:137], v[90:93], v[78:81]
	ds_read_b128 v[114:117], v161 offset:2048
	v_mfma_f32_16x16x32_f16 v[22:25], v[138:141], v[90:93], v[22:25]
	ds_read_b128 v[118:121], v161 offset:4096
	v_mfma_f32_16x16x32_f16 v[30:33], v[142:145], v[90:93], v[30:33]
	ds_read_b128 v[122:125], v161 offset:6144
	v_mfma_f32_16x16x32_f16 v[74:77], v[134:137], v[94:97], v[74:77]
	ds_read_b128 v[126:129], v161 offset:8192
	v_mfma_f32_16x16x32_f16 v[18:21], v[138:141], v[94:97], v[18:21]
	ds_read_b128 v[130:133], v161 offset:10240
	v_mfma_f32_16x16x32_f16 v[26:29], v[142:145], v[94:97], v[26:29]
	v_mfma_f32_16x16x32_f16 v[70:73], v[134:137], v[98:101], v[70:73]
	v_mfma_f32_16x16x32_f16 v[46:49], v[138:141], v[98:101], v[46:49]
	v_mfma_f32_16x16x32_f16 v[240:243], v[142:145], v[98:101], v[240:243]
	v_mfma_f32_16x16x32_f16 v[66:69], v[134:137], v[102:105], v[66:69]
	v_mfma_f32_16x16x32_f16 v[42:45], v[138:141], v[102:105], v[42:45]
	v_mfma_f32_16x16x32_f16 v[236:239], v[142:145], v[102:105], v[236:239]
	v_mfma_f32_16x16x32_f16 v[62:65], v[134:137], v[106:109], v[62:65]
	v_mfma_f32_16x16x32_f16 v[38:41], v[138:141], v[106:109], v[38:41]
	v_mfma_f32_16x16x32_f16 v[34:37], v[142:145], v[106:109], v[34:37]
	s_waitcnt vmcnt(3) lgkmcnt(0)
	s_barrier
	ds_read_b128 v[134:137], v162
	v_mfma_f32_16x16x32_f16 v[82:85], v[146:149], v[110:113], v[82:85]
	ds_read_b128 v[138:141], v162 offset:2048
	v_mfma_f32_16x16x32_f16 v[58:61], v[150:153], v[110:113], v[58:61]
	ds_read_b128 v[142:145], v162 offset:4096
	v_mfma_f32_16x16x32_f16 v[14:17], v[154:157], v[110:113], v[14:17]
	ds_read_b128 v[86:89], v158
	v_mfma_f32_16x16x32_f16 v[78:81], v[146:149], v[114:117], v[78:81]
	ds_read_b128 v[90:93], v158 offset:2048
	v_mfma_f32_16x16x32_f16 v[22:25], v[150:153], v[114:117], v[22:25]
	ds_read_b128 v[94:97], v158 offset:4096
	v_mfma_f32_16x16x32_f16 v[30:33], v[154:157], v[114:117], v[30:33]
	ds_read_b128 v[98:101], v158 offset:6144
	v_mfma_f32_16x16x32_f16 v[74:77], v[146:149], v[118:121], v[74:77]
	ds_read_b128 v[102:105], v158 offset:8192
	v_mfma_f32_16x16x32_f16 v[18:21], v[150:153], v[118:121], v[18:21]
	ds_read_b128 v[106:109], v158 offset:10240
	v_mfma_f32_16x16x32_f16 v[26:29], v[154:157], v[118:121], v[26:29]
	v_mfma_f32_16x16x32_f16 v[70:73], v[146:149], v[122:125], v[70:73]
	v_mfma_f32_16x16x32_f16 v[46:49], v[150:153], v[122:125], v[46:49]
	v_mfma_f32_16x16x32_f16 v[240:243], v[154:157], v[122:125], v[240:243]
	v_mfma_f32_16x16x32_f16 v[66:69], v[146:149], v[126:129], v[66:69]
	v_mfma_f32_16x16x32_f16 v[42:45], v[150:153], v[126:129], v[42:45]
	v_mfma_f32_16x16x32_f16 v[236:239], v[154:157], v[126:129], v[236:239]
	v_mfma_f32_16x16x32_f16 v[62:65], v[146:149], v[130:133], v[62:65]
	v_mfma_f32_16x16x32_f16 v[38:41], v[150:153], v[130:133], v[38:41]
	v_mfma_f32_16x16x32_f16 v[34:37], v[154:157], v[130:133], v[34:37]
	s_waitcnt lgkmcnt(0)
	ds_read_b128 v[146:149], v164
	v_mfma_f32_16x16x32_f16 v[82:85], v[134:137], v[86:89], v[82:85]
	ds_read_b128 v[150:153], v164 offset:2048
	v_mfma_f32_16x16x32_f16 v[58:61], v[138:141], v[86:89], v[58:61]
	ds_read_b128 v[154:157], v164 offset:4096
	v_mfma_f32_16x16x32_f16 v[14:17], v[142:145], v[86:89], v[14:17]
	ds_read_b128 v[110:113], v160
	v_mfma_f32_16x16x32_f16 v[78:81], v[134:137], v[90:93], v[78:81]
	ds_read_b128 v[114:117], v160 offset:2048
	v_mfma_f32_16x16x32_f16 v[22:25], v[138:141], v[90:93], v[22:25]
	ds_read_b128 v[118:121], v160 offset:4096
	v_mfma_f32_16x16x32_f16 v[30:33], v[142:145], v[90:93], v[30:33]
	ds_read_b128 v[122:125], v160 offset:6144
	v_mfma_f32_16x16x32_f16 v[74:77], v[134:137], v[94:97], v[74:77]
	ds_read_b128 v[126:129], v160 offset:8192
	v_mfma_f32_16x16x32_f16 v[18:21], v[138:141], v[94:97], v[18:21]
	ds_read_b128 v[130:133], v160 offset:10240
	v_mfma_f32_16x16x32_f16 v[26:29], v[142:145], v[94:97], v[26:29]
	v_mfma_f32_16x16x32_f16 v[70:73], v[134:137], v[98:101], v[70:73]
	v_mfma_f32_16x16x32_f16 v[46:49], v[138:141], v[98:101], v[46:49]
	v_mfma_f32_16x16x32_f16 v[240:243], v[142:145], v[98:101], v[240:243]
	v_mfma_f32_16x16x32_f16 v[66:69], v[134:137], v[102:105], v[66:69]
	v_mfma_f32_16x16x32_f16 v[42:45], v[138:141], v[102:105], v[42:45]
	v_mfma_f32_16x16x32_f16 v[236:239], v[142:145], v[102:105], v[236:239]
	v_mfma_f32_16x16x32_f16 v[62:65], v[134:137], v[106:109], v[62:65]
	v_mfma_f32_16x16x32_f16 v[38:41], v[138:141], v[106:109], v[38:41]
	v_mfma_f32_16x16x32_f16 v[34:37], v[142:145], v[106:109], v[34:37]
	s_waitcnt lgkmcnt(0)
	v_mfma_f32_16x16x32_f16 v[82:85], v[146:149], v[110:113], v[82:85]
	v_mfma_f32_16x16x32_f16 v[58:61], v[150:153], v[110:113], v[58:61]
	v_mfma_f32_16x16x32_f16 v[14:17], v[154:157], v[110:113], v[14:17]
	v_mfma_f32_16x16x32_f16 v[78:81], v[146:149], v[114:117], v[78:81]
	v_mfma_f32_16x16x32_f16 v[22:25], v[150:153], v[114:117], v[22:25]
	v_mfma_f32_16x16x32_f16 v[30:33], v[154:157], v[114:117], v[30:33]
	v_mfma_f32_16x16x32_f16 v[74:77], v[146:149], v[118:121], v[74:77]
	v_mfma_f32_16x16x32_f16 v[18:21], v[150:153], v[118:121], v[18:21]
	v_mfma_f32_16x16x32_f16 v[26:29], v[154:157], v[118:121], v[26:29]
	v_mfma_f32_16x16x32_f16 v[70:73], v[146:149], v[122:125], v[70:73]
	v_mfma_f32_16x16x32_f16 v[46:49], v[150:153], v[122:125], v[46:49]
	v_mfma_f32_16x16x32_f16 v[240:243], v[154:157], v[122:125], v[240:243]
	v_mfma_f32_16x16x32_f16 v[66:69], v[146:149], v[126:129], v[66:69]
	v_mfma_f32_16x16x32_f16 v[42:45], v[150:153], v[126:129], v[42:45]
	v_mfma_f32_16x16x32_f16 v[236:239], v[154:157], v[126:129], v[236:239]
	v_mfma_f32_16x16x32_f16 v[62:65], v[146:149], v[130:133], v[62:65]
	v_mfma_f32_16x16x32_f16 v[38:41], v[150:153], v[130:133], v[38:41]
	v_mfma_f32_16x16x32_f16 v[34:37], v[154:157], v[130:133], v[34:37]
	s_branch .LBB1_76
.Lgemm_N_loop:
	s_waitcnt lgkmcnt(0)
	ds_read_b128 v[146:149], v164
	v_mfma_f32_16x16x32_f16 v[82:85], v[86:89], v[134:137], v[82:85]
	s_add_u32 m0, s11, 0x1e080
	ds_read_b128 v[150:153], v164 offset:2048
	global_load_lds_dwordx4 v[220:221], off offset:-128
	v_mfma_f32_16x16x32_f16 v[58:61], v[86:89], v[138:141], v[58:61]
	ds_read_b128 v[154:157], v164 offset:4096
	v_mfma_f32_16x16x32_f16 v[14:17], v[86:89], v[142:145], v[14:17]
	ds_read_b128 v[110:113], v160
	v_mfma_f32_16x16x32_f16 v[78:81], v[90:93], v[134:137], v[78:81]
	ds_read_b128 v[114:117], v160 offset:2048
	v_mfma_f32_16x16x32_f16 v[22:25], v[90:93], v[138:141], v[22:25]
	ds_read_b128 v[118:121], v160 offset:4096
	v_mfma_f32_16x16x32_f16 v[30:33], v[90:93], v[142:145], v[30:33]
	ds_read_b128 v[122:125], v160 offset:6144
	v_mfma_f32_16x16x32_f16 v[74:77], v[94:97], v[134:137], v[74:77]
	s_add_u32 m0, s11, 0x20080
	ds_read_b128 v[126:129], v160 offset:8192
	global_load_lds_dwordx4 v[224:225], off offset:-128
	v_mfma_f32_16x16x32_f16 v[18:21], v[94:97], v[138:141], v[18:21]
	ds_read_b128 v[130:133], v160 offset:10240
	v_mfma_f32_16x16x32_f16 v[26:29], v[94:97], v[142:145], v[26:29]
	v_mfma_f32_16x16x32_f16 v[70:73], v[98:101], v[134:137], v[70:73]
	v_mfma_f32_16x16x32_f16 v[46:49], v[98:101], v[138:141], v[46:49]
	v_mfma_f32_16x16x32_f16 v[240:243], v[98:101], v[142:145], v[240:243]
	v_mfma_f32_16x16x32_f16 v[66:69], v[102:105], v[134:137], v[66:69]
	s_add_u32 m0, s11, 0x22080
	v_mfma_f32_16x16x32_f16 v[42:45], v[102:105], v[138:141], v[42:45]
	global_load_lds_dwordx4 v[228:229], off offset:-128
	v_mfma_f32_16x16x32_f16 v[236:239], v[102:105], v[142:145], v[236:239]
	v_mfma_f32_16x16x32_f16 v[62:65], v[106:109], v[134:137], v[62:65]
	v_mfma_f32_16x16x32_f16 v[38:41], v[106:109], v[138:141], v[38:41]
	v_mfma_f32_16x16x32_f16 v[34:37], v[106:109], v[142:145], v[34:37]
	s_waitcnt vmcnt(6) lgkmcnt(0)
	s_barrier
	ds_read_b128 v[134:137], v162 offset:49152
	v_mfma_f32_16x16x32_f16 v[82:85], v[110:113], v[146:149], v[82:85]
	s_add_u32 m0, s11, 0x0
	ds_read_b128 v[138:141], v162 offset:51200
	global_load_lds_dwordx4 v[218:219], off
	v_mfma_f32_16x16x32_f16 v[58:61], v[110:113], v[150:153], v[58:61]
	ds_read_b128 v[142:145], v162 offset:53248
	v_mfma_f32_16x16x32_f16 v[14:17], v[110:113], v[154:157], v[14:17]
	ds_read_b128 v[86:89], v158 offset:49152
	v_mfma_f32_16x16x32_f16 v[78:81], v[114:117], v[146:149], v[78:81]
	ds_read_b128 v[90:93], v158 offset:51200
	v_mfma_f32_16x16x32_f16 v[22:25], v[114:117], v[150:153], v[22:25]
	ds_read_b128 v[94:97], v158 offset:53248
	v_mfma_f32_16x16x32_f16 v[30:33], v[114:117], v[154:157], v[30:33]
	ds_read_b128 v[98:101], v158 offset:55296
	v_mfma_f32_16x16x32_f16 v[74:77], v[118:121], v[146:149], v[74:77]
	s_add_u32 m0, s11, 0x2000
	ds_read_b128 v[102:105], v158 offset:57344
	global_load_lds_dwordx4 v[222:223], off
	v_mfma_f32_16x16x32_f16 v[18:21], v[118:121], v[150:153], v[18:21]
	ds_read_b128 v[106:109], v158 offset:59392
	v_mfma_f32_16x16x32_f16 v[26:29], v[118:121], v[154:157], v[26:29]
	v_mfma_f32_16x16x32_f16 v[70:73], v[122:125], v[146:149], v[70:73]
	v_mfma_f32_16x16x32_f16 v[46:49], v[122:125], v[150:153], v[46:49]
	v_mfma_f32_16x16x32_f16 v[240:243], v[122:125], v[154:157], v[240:243]
	v_mfma_f32_16x16x32_f16 v[66:69], v[126:129], v[146:149], v[66:69]
	s_add_u32 m0, s11, 0x4000
	v_mfma_f32_16x16x32_f16 v[42:45], v[126:129], v[150:153], v[42:45]
	global_load_lds_dwordx4 v[226:227], off
	v_mfma_f32_16x16x32_f16 v[236:239], v[126:129], v[154:157], v[236:239]
	v_mfma_f32_16x16x32_f16 v[62:65], v[130:133], v[146:149], v[62:65]
	v_mfma_f32_16x16x32_f16 v[38:41], v[130:133], v[150:153], v[38:41]
	v_mfma_f32_16x16x32_f16 v[34:37], v[130:133], v[154:157], v[34:37]
	s_waitcnt lgkmcnt(0)
	ds_read_b128 v[146:149], v164 offset:49152
	v_mfma_f32_16x16x32_f16 v[82:85], v[86:89], v[134:137], v[82:85]
	s_add_u32 m0, s11, 0x6000
	ds_read_b128 v[150:153], v164 offset:51200
	global_load_lds_dwordx4 v[220:221], off
	v_mfma_f32_16x16x32_f16 v[58:61], v[86:89], v[138:141], v[58:61]
	ds_read_b128 v[154:157], v164 offset:53248
	v_mfma_f32_16x16x32_f16 v[14:17], v[86:89], v[142:145], v[14:17]
	ds_read_b128 v[110:113], v160 offset:49152
	v_mfma_f32_16x16x32_f16 v[78:81], v[90:93], v[134:137], v[78:81]
	ds_read_b128 v[114:117], v160 offset:51200
	v_mfma_f32_16x16x32_f16 v[22:25], v[90:93], v[138:141], v[22:25]
	ds_read_b128 v[118:121], v160 offset:53248
	v_mfma_f32_16x16x32_f16 v[30:33], v[90:93], v[142:145], v[30:33]
	ds_read_b128 v[122:125], v160 offset:55296
	v_mfma_f32_16x16x32_f16 v[74:77], v[94:97], v[134:137], v[74:77]
	s_add_u32 m0, s11, 0x8000
	ds_read_b128 v[126:129], v160 offset:57344
	global_load_lds_dwordx4 v[224:225], off
	v_mfma_f32_16x16x32_f16 v[18:21], v[94:97], v[138:141], v[18:21]
	ds_read_b128 v[130:133], v160 offset:59392
	v_mfma_f32_16x16x32_f16 v[26:29], v[94:97], v[142:145], v[26:29]
	v_mfma_f32_16x16x32_f16 v[70:73], v[98:101], v[134:137], v[70:73]
	v_mfma_f32_16x16x32_f16 v[46:49], v[98:101], v[138:141], v[46:49]
	v_mfma_f32_16x16x32_f16 v[240:243], v[98:101], v[142:145], v[240:243]
	v_mfma_f32_16x16x32_f16 v[66:69], v[102:105], v[134:137], v[66:69]
	s_add_u32 m0, s11, 0xa000
	v_mfma_f32_16x16x32_f16 v[42:45], v[102:105], v[138:141], v[42:45]
	global_load_lds_dwordx4 v[228:229], off
	v_mfma_f32_16x16x32_f16 v[236:239], v[102:105], v[142:145], v[236:239]
	v_mfma_f32_16x16x32_f16 v[62:65], v[106:109], v[134:137], v[62:65]
	v_mfma_f32_16x16x32_f16 v[38:41], v[106:109], v[138:141], v[38:41]
	v_mfma_f32_16x16x32_f16 v[34:37], v[106:109], v[142:145], v[34:37]
	s_waitcnt vmcnt(6) lgkmcnt(0)
	s_barrier
	ds_read_b128 v[134:137], v163
	v_mfma_f32_16x16x32_f16 v[82:85], v[110:113], v[146:149], v[82:85]
	s_add_u32 m0, s11, 0xbf80
	ds_read_b128 v[138:141], v163 offset:2048
	global_load_lds_dwordx4 v[218:219], off offset:128
	v_mfma_f32_16x16x32_f16 v[58:61], v[110:113], v[150:153], v[58:61]
	ds_read_b128 v[142:145], v163 offset:4096
	v_mfma_f32_16x16x32_f16 v[14:17], v[110:113], v[154:157], v[14:17]
	ds_read_b128 v[86:89], v159
	v_mfma_f32_16x16x32_f16 v[78:81], v[114:117], v[146:149], v[78:81]
	ds_read_b128 v[90:93], v159 offset:2048
	v_mfma_f32_16x16x32_f16 v[22:25], v[114:117], v[150:153], v[22:25]
	ds_read_b128 v[94:97], v159 offset:4096
	v_mfma_f32_16x16x32_f16 v[30:33], v[114:117], v[154:157], v[30:33]
	ds_read_b128 v[98:101], v159 offset:6144
	v_mfma_f32_16x16x32_f16 v[74:77], v[118:121], v[146:149], v[74:77]
	s_add_u32 m0, s11, 0xdf80
	ds_read_b128 v[102:105], v159 offset:8192
	global_load_lds_dwordx4 v[222:223], off offset:128
	v_mfma_f32_16x16x32_f16 v[18:21], v[118:121], v[150:153], v[18:21]
	ds_read_b128 v[106:109], v159 offset:10240
	v_mfma_f32_16x16x32_f16 v[26:29], v[118:121], v[154:157], v[26:29]
	v_mfma_f32_16x16x32_f16 v[70:73], v[122:125], v[146:149], v[70:73]
	v_mfma_f32_16x16x32_f16 v[46:49], v[122:125], v[150:153], v[46:49]
	v_mfma_f32_16x16x32_f16 v[240:243], v[122:125], v[154:157], v[240:243]
	v_mfma_f32_16x16x32_f16 v[66:69], v[126:129], v[146:149], v[66:69]
	s_add_u32 m0, s11, 0xff80
	v_mfma_f32_16x16x32_f16 v[42:45], v[126:129], v[150:153], v[42:45]
	global_load_lds_dwordx4 v[226:227], off offset:128
	v_mfma_f32_16x16x32_f16 v[236:239], v[126:129], v[154:157], v[236:239]
	v_mfma_f32_16x16x32_f16 v[62:65], v[130:133], v[146:149], v[62:65]
	v_mfma_f32_16x16x32_f16 v[38:41], v[130:133], v[150:153], v[38:41]
	v_mfma_f32_16x16x32_f16 v[34:37], v[130:133], v[154:157], v[34:37]
	s_waitcnt lgkmcnt(0)
	ds_read_b128 v[146:149], v165
	v_mfma_f32_16x16x32_f16 v[82:85], v[86:89], v[134:137], v[82:85]
	s_add_u32 m0, s11, 0x11f80
	ds_read_b128 v[150:153], v165 offset:2048
	global_load_lds_dwordx4 v[220:221], off offset:128
	v_mfma_f32_16x16x32_f16 v[58:61], v[86:89], v[138:141], v[58:61]
	ds_read_b128 v[154:157], v165 offset:4096
	v_mfma_f32_16x16x32_f16 v[14:17], v[86:89], v[142:145], v[14:17]
	ds_read_b128 v[110:113], v161
	v_mfma_f32_16x16x32_f16 v[78:81], v[90:93], v[134:137], v[78:81]
	ds_read_b128 v[114:117], v161 offset:2048
	v_mfma_f32_16x16x32_f16 v[22:25], v[90:93], v[138:141], v[22:25]
	ds_read_b128 v[118:121], v161 offset:4096
	v_mfma_f32_16x16x32_f16 v[30:33], v[90:93], v[142:145], v[30:33]
	ds_read_b128 v[122:125], v161 offset:6144
	v_mfma_f32_16x16x32_f16 v[74:77], v[94:97], v[134:137], v[74:77]
	s_add_u32 m0, s11, 0x13f80
	ds_read_b128 v[126:129], v161 offset:8192
	global_load_lds_dwordx4 v[224:225], off offset:128
	v_mfma_f32_16x16x32_f16 v[18:21], v[94:97], v[138:141], v[18:21]
	ds_read_b128 v[130:133], v161 offset:10240
	v_mfma_f32_16x16x32_f16 v[26:29], v[94:97], v[142:145], v[26:29]
	v_mfma_f32_16x16x32_f16 v[70:73], v[98:101], v[134:137], v[70:73]
	v_mfma_f32_16x16x32_f16 v[46:49], v[98:101], v[138:141], v[46:49]
	v_mfma_f32_16x16x32_f16 v[240:243], v[98:101], v[142:145], v[240:243]
	v_mfma_f32_16x16x32_f16 v[66:69], v[102:105], v[134:137], v[66:69]
	s_add_u32 m0, s11, 0x15f80
	v_mfma_f32_16x16x32_f16 v[42:45], v[102:105], v[138:141], v[42:45]
	global_load_lds_dwordx4 v[228:229], off offset:128
	v_mfma_f32_16x16x32_f16 v[236:239], v[102:105], v[142:145], v[236:239]
	v_mfma_f32_16x16x32_f16 v[62:65], v[106:109], v[134:137], v[62:65]
	v_mfma_f32_16x16x32_f16 v[38:41], v[106:109], v[138:141], v[38:41]
	v_mfma_f32_16x16x32_f16 v[34:37], v[106:109], v[142:145], v[34:37]
	s_waitcnt vmcnt(6) lgkmcnt(0)
	s_barrier
	ds_read_b128 v[134:137], v162
	v_mfma_f32_16x16x32_f16 v[82:85], v[110:113], v[146:149], v[82:85]
	s_add_u32 m0, s11, 0x17f00
	ds_read_b128 v[138:141], v162 offset:2048
	global_load_lds_dwordx4 v[218:219], off offset:256
	v_mfma_f32_16x16x32_f16 v[58:61], v[110:113], v[150:153], v[58:61]
	ds_read_b128 v[142:145], v162 offset:4096
	v_mfma_f32_16x16x32_f16 v[14:17], v[110:113], v[154:157], v[14:17]
	ds_read_b128 v[86:89], v158
	v_mfma_f32_16x16x32_f16 v[78:81], v[114:117], v[146:149], v[78:81]
	ds_read_b128 v[90:93], v158 offset:2048
	v_mfma_f32_16x16x32_f16 v[22:25], v[114:117], v[150:153], v[22:25]
	ds_read_b128 v[94:97], v158 offset:4096
	v_mfma_f32_16x16x32_f16 v[30:33], v[114:117], v[154:157], v[30:33]
	ds_read_b128 v[98:101], v158 offset:6144
	v_mfma_f32_16x16x32_f16 v[74:77], v[118:121], v[146:149], v[74:77]
	s_add_u32 m0, s11, 0x19f00
	ds_read_b128 v[102:105], v158 offset:8192
	global_load_lds_dwordx4 v[222:223], off offset:256
	v_mfma_f32_16x16x32_f16 v[18:21], v[118:121], v[150:153], v[18:21]
	ds_read_b128 v[106:109], v158 offset:10240
	v_mfma_f32_16x16x32_f16 v[26:29], v[118:121], v[154:157], v[26:29]
	v_mfma_f32_16x16x32_f16 v[70:73], v[122:125], v[146:149], v[70:73]
	v_mfma_f32_16x16x32_f16 v[46:49], v[122:125], v[150:153], v[46:49]
	v_mfma_f32_16x16x32_f16 v[240:243], v[122:125], v[154:157], v[240:243]
	v_mfma_f32_16x16x32_f16 v[66:69], v[126:129], v[146:149], v[66:69]
	s_add_u32 m0, s11, 0x1bf00
	v_mfma_f32_16x16x32_f16 v[42:45], v[126:129], v[150:153], v[42:45]
	global_load_lds_dwordx4 v[226:227], off offset:256
	v_mfma_f32_16x16x32_f16 v[236:239], v[126:129], v[154:157], v[236:239]
	v_mfma_f32_16x16x32_f16 v[62:65], v[130:133], v[146:149], v[62:65]
	v_mfma_f32_16x16x32_f16 v[38:41], v[130:133], v[150:153], v[38:41]
	v_mfma_f32_16x16x32_f16 v[34:37], v[130:133], v[154:157], v[34:37]
	v_lshl_add_u64 v[218:219], v[218:219], 0, s[20:21]
	v_lshl_add_u64 v[222:223], v[222:223], 0, s[20:21]
	v_lshl_add_u64 v[226:227], v[226:227], 0, s[20:21]
	v_lshl_add_u64 v[220:221], v[220:221], 0, s[20:21]
	v_lshl_add_u64 v[224:225], v[224:225], 0, s[20:21]
	v_lshl_add_u64 v[228:229], v[228:229], 0, s[20:21]
	s_sub_u32 s22, s22, 1
	s_cmp_lg_u32 s22, 0
	s_cbranch_scc1 .Lgemm_N_loop
	s_waitcnt lgkmcnt(0)
	ds_read_b128 v[146:149], v164
	v_mfma_f32_16x16x32_f16 v[82:85], v[86:89], v[134:137], v[82:85]
	s_add_u32 m0, s11, 0x1e080
	ds_read_b128 v[150:153], v164 offset:2048
	global_load_lds_dwordx4 v[220:221], off offset:-128
	v_mfma_f32_16x16x32_f16 v[58:61], v[86:89], v[138:141], v[58:61]
	ds_read_b128 v[154:157], v164 offset:4096
	v_mfma_f32_16x16x32_f16 v[14:17], v[86:89], v[142:145], v[14:17]
	ds_read_b128 v[110:113], v160
	v_mfma_f32_16x16x32_f16 v[78:81], v[90:93], v[134:137], v[78:81]
	ds_read_b128 v[114:117], v160 offset:2048
	v_mfma_f32_16x16x32_f16 v[22:25], v[90:93], v[138:141], v[22:25]
	ds_read_b128 v[118:121], v160 offset:4096
	v_mfma_f32_16x16x32_f16 v[30:33], v[90:93], v[142:145], v[30:33]
	ds_read_b128 v[122:125], v160 offset:6144
	v_mfma_f32_16x16x32_f16 v[74:77], v[94:97], v[134:137], v[74:77]
	s_add_u32 m0, s11, 0x20080
	ds_read_b128 v[126:129], v160 offset:8192
	global_load_lds_dwordx4 v[224:225], off offset:-128
	v_mfma_f32_16x16x32_f16 v[18:21], v[94:97], v[138:141], v[18:21]
	ds_read_b128 v[130:133], v160 offset:10240
	v_mfma_f32_16x16x32_f16 v[26:29], v[94:97], v[142:145], v[26:29]
	v_mfma_f32_16x16x32_f16 v[70:73], v[98:101], v[134:137], v[70:73]
	v_mfma_f32_16x16x32_f16 v[46:49], v[98:101], v[138:141], v[46:49]
	v_mfma_f32_16x16x32_f16 v[240:243], v[98:101], v[142:145], v[240:243]
	v_mfma_f32_16x16x32_f16 v[66:69], v[102:105], v[134:137], v[66:69]
	s_add_u32 m0, s11, 0x22080
	v_mfma_f32_16x16x32_f16 v[42:45], v[102:105], v[138:141], v[42:45]
	global_load_lds_dwordx4 v[228:229], off offset:-128
	v_mfma_f32_16x16x32_f16 v[236:239], v[102:105], v[142:145], v[236:239]
	v_mfma_f32_16x16x32_f16 v[62:65], v[106:109], v[134:137], v[62:65]
	v_mfma_f32_16x16x32_f16 v[38:41], v[106:109], v[138:141], v[38:41]
	v_mfma_f32_16x16x32_f16 v[34:37], v[106:109], v[142:145], v[34:37]
	s_waitcnt vmcnt(6) lgkmcnt(0)
	s_barrier
	ds_read_b128 v[134:137], v162 offset:49152
	v_mfma_f32_16x16x32_f16 v[82:85], v[110:113], v[146:149], v[82:85]
	s_add_u32 m0, s11, 0x0
	ds_read_b128 v[138:141], v162 offset:51200
	global_load_lds_dwordx4 v[218:219], off
	v_mfma_f32_16x16x32_f16 v[58:61], v[110:113], v[150:153], v[58:61]
	ds_read_b128 v[142:145], v162 offset:53248
	v_mfma_f32_16x16x32_f16 v[14:17], v[110:113], v[154:157], v[14:17]
	ds_read_b128 v[86:89], v158 offset:49152
	v_mfma_f32_16x16x32_f16 v[78:81], v[114:117], v[146:149], v[78:81]
	ds_read_b128 v[90:93], v158 offset:51200
	v_mfma_f32_16x16x32_f16 v[22:25], v[114:117], v[150:153], v[22:25]
	ds_read_b128 v[94:97], v158 offset:53248
	v_mfma_f32_16x16x32_f16 v[30:33], v[114:117], v[154:157], v[30:33]
	ds_read_b128 v[98:101], v158 offset:55296
	v_mfma_f32_16x16x32_f16 v[74:77], v[118:121], v[146:149], v[74:77]
	s_add_u32 m0, s11, 0x2000
	ds_read_b128 v[102:105], v158 offset:57344
	global_load_lds_dwordx4 v[222:223], off
	v_mfma_f32_16x16x32_f16 v[18:21], v[118:121], v[150:153], v[18:21]
	ds_read_b128 v[106:109], v158 offset:59392
	v_mfma_f32_16x16x32_f16 v[26:29], v[118:121], v[154:157], v[26:29]
	v_mfma_f32_16x16x32_f16 v[70:73], v[122:125], v[146:149], v[70:73]
	v_mfma_f32_16x16x32_f16 v[46:49], v[122:125], v[150:153], v[46:49]
	v_mfma_f32_16x16x32_f16 v[240:243], v[122:125], v[154:157], v[240:243]
	v_mfma_f32_16x16x32_f16 v[66:69], v[126:129], v[146:149], v[66:69]
	s_add_u32 m0, s11, 0x4000
	v_mfma_f32_16x16x32_f16 v[42:45], v[126:129], v[150:153], v[42:45]
	global_load_lds_dwordx4 v[226:227], off
	v_mfma_f32_16x16x32_f16 v[236:239], v[126:129], v[154:157], v[236:239]
	v_mfma_f32_16x16x32_f16 v[62:65], v[130:133], v[146:149], v[62:65]
	v_mfma_f32_16x16x32_f16 v[38:41], v[130:133], v[150:153], v[38:41]
	v_mfma_f32_16x16x32_f16 v[34:37], v[130:133], v[154:157], v[34:37]
	s_waitcnt lgkmcnt(0)
	ds_read_b128 v[146:149], v164 offset:49152
	v_mfma_f32_16x16x32_f16 v[82:85], v[86:89], v[134:137], v[82:85]
	s_add_u32 m0, s11, 0x6000
	ds_read_b128 v[150:153], v164 offset:51200
	global_load_lds_dwordx4 v[220:221], off
	v_mfma_f32_16x16x32_f16 v[58:61], v[86:89], v[138:141], v[58:61]
	ds_read_b128 v[154:157], v164 offset:53248
	v_mfma_f32_16x16x32_f16 v[14:17], v[86:89], v[142:145], v[14:17]
	ds_read_b128 v[110:113], v160 offset:49152
	v_mfma_f32_16x16x32_f16 v[78:81], v[90:93], v[134:137], v[78:81]
	ds_read_b128 v[114:117], v160 offset:51200
	v_mfma_f32_16x16x32_f16 v[22:25], v[90:93], v[138:141], v[22:25]
	ds_read_b128 v[118:121], v160 offset:53248
	v_mfma_f32_16x16x32_f16 v[30:33], v[90:93], v[142:145], v[30:33]
	ds_read_b128 v[122:125], v160 offset:55296
	v_mfma_f32_16x16x32_f16 v[74:77], v[94:97], v[134:137], v[74:77]
	s_add_u32 m0, s11, 0x8000
	ds_read_b128 v[126:129], v160 offset:57344
	global_load_lds_dwordx4 v[224:225], off
	v_mfma_f32_16x16x32_f16 v[18:21], v[94:97], v[138:141], v[18:21]
	ds_read_b128 v[130:133], v160 offset:59392
	v_mfma_f32_16x16x32_f16 v[26:29], v[94:97], v[142:145], v[26:29]
	v_mfma_f32_16x16x32_f16 v[70:73], v[98:101], v[134:137], v[70:73]
	v_mfma_f32_16x16x32_f16 v[46:49], v[98:101], v[138:141], v[46:49]
	v_mfma_f32_16x16x32_f16 v[240:243], v[98:101], v[142:145], v[240:243]
	v_mfma_f32_16x16x32_f16 v[66:69], v[102:105], v[134:137], v[66:69]
	s_add_u32 m0, s11, 0xa000
	v_mfma_f32_16x16x32_f16 v[42:45], v[102:105], v[138:141], v[42:45]
	global_load_lds_dwordx4 v[228:229], off
	v_mfma_f32_16x16x32_f16 v[236:239], v[102:105], v[142:145], v[236:239]
	v_mfma_f32_16x16x32_f16 v[62:65], v[106:109], v[134:137], v[62:65]
	v_mfma_f32_16x16x32_f16 v[38:41], v[106:109], v[138:141], v[38:41]
	v_mfma_f32_16x16x32_f16 v[34:37], v[106:109], v[142:145], v[34:37]
	s_waitcnt vmcnt(6) lgkmcnt(0)
	s_barrier
	s_lshl_b32 s26, s17, 2
	s_add_u32 s26, s24, s26
	s_addc_u32 s27, s25, 0
	v_lshlrev_b32_e32 v50, 2, v1
	global_load_dword v234, v50, s[26:27]
	global_load_dword v232, v50, s[26:27] offset:64
	global_load_dword v230, v50, s[26:27] offset:128
	ds_read_b128 v[134:137], v163
	v_mfma_f32_16x16x32_f16 v[82:85], v[110:113], v[146:149], v[82:85]
	ds_read_b128 v[138:141], v163 offset:2048
	v_mfma_f32_16x16x32_f16 v[58:61], v[110:113], v[150:153], v[58:61]
	ds_read_b128 v[142:145], v163 offset:4096
	v_mfma_f32_16x16x32_f16 v[14:17], v[110:113], v[154:157], v[14:17]
	ds_read_b128 v[86:89], v159
	v_mfma_f32_16x16x32_f16 v[78:81], v[114:117], v[146:149], v[78:81]
	ds_read_b128 v[90:93], v159 offset:2048
	v_mfma_f32_16x16x32_f16 v[22:25], v[114:117], v[150:153], v[22:25]
	ds_read_b128 v[94:97], v159 offset:4096
	v_mfma_f32_16x16x32_f16 v[30:33], v[114:117], v[154:157], v[30:33]
	ds_read_b128 v[98:101], v159 offset:6144
	v_mfma_f32_16x16x32_f16 v[74:77], v[118:121], v[146:149], v[74:77]
	ds_read_b128 v[102:105], v159 offset:8192
	v_mfma_f32_16x16x32_f16 v[18:21], v[118:121], v[150:153], v[18:21]
	ds_read_b128 v[106:109], v159 offset:10240
	v_mfma_f32_16x16x32_f16 v[26:29], v[118:121], v[154:157], v[26:29]
	v_mfma_f32_16x16x32_f16 v[70:73], v[122:125], v[146:149], v[70:73]
	v_mfma_f32_16x16x32_f16 v[46:49], v[122:125], v[150:153], v[46:49]
	v_mfma_f32_16x16x32_f16 v[240:243], v[122:125], v[154:157], v[240:243]
	v_mfma_f32_16x16x32_f16 v[66:69], v[126:129], v[146:149], v[66:69]
	v_mfma_f32_16x16x32_f16 v[42:45], v[126:129], v[150:153], v[42:45]
	v_mfma_f32_16x16x32_f16 v[236:239], v[126:129], v[154:157], v[236:239]
	v_mfma_f32_16x16x32_f16 v[62:65], v[130:133], v[146:149], v[62:65]
	v_mfma_f32_16x16x32_f16 v[38:41], v[130:133], v[150:153], v[38:41]
	v_mfma_f32_16x16x32_f16 v[34:37], v[130:133], v[154:157], v[34:37]
	s_waitcnt lgkmcnt(0)
	ds_read_b128 v[146:149], v165
	v_mfma_f32_16x16x32_f16 v[82:85], v[86:89], v[134:137], v[82:85]
	ds_read_b128 v[150:153], v165 offset:2048
	v_mfma_f32_16x16x32_f16 v[58:61], v[86:89], v[138:141], v[58:61]
	ds_read_b128 v[154:157], v165 offset:4096
	v_mfma_f32_16x16x32_f16 v[14:17], v[86:89], v[142:145], v[14:17]
	ds_read_b128 v[110:113], v161
	v_mfma_f32_16x16x32_f16 v[78:81], v[90:93], v[134:137], v[78:81]
	ds_read_b128 v[114:117], v161 offset:2048
	v_mfma_f32_16x16x32_f16 v[22:25], v[90:93], v[138:141], v[22:25]
	ds_read_b128 v[118:121], v161 offset:4096
	v_mfma_f32_16x16x32_f16 v[30:33], v[90:93], v[142:145], v[30:33]
	ds_read_b128 v[122:125], v161 offset:6144
	v_mfma_f32_16x16x32_f16 v[74:77], v[94:97], v[134:137], v[74:77]
	ds_read_b128 v[126:129], v161 offset:8192
	v_mfma_f32_16x16x32_f16 v[18:21], v[94:97], v[138:141], v[18:21]
	ds_read_b128 v[130:133], v161 offset:10240
	v_mfma_f32_16x16x32_f16 v[26:29], v[94:97], v[142:145], v[26:29]
	v_mfma_f32_16x16x32_f16 v[70:73], v[98:101], v[134:137], v[70:73]
	v_mfma_f32_16x16x32_f16 v[46:49], v[98:101], v[138:141], v[46:49]
	v_mfma_f32_16x16x32_f16 v[240:243], v[98:101], v[142:145], v[240:243]
	v_mfma_f32_16x16x32_f16 v[66:69], v[102:105], v[134:137], v[66:69]
	v_mfma_f32_16x16x32_f16 v[42:45], v[102:105], v[138:141], v[42:45]
	v_mfma_f32_16x16x32_f16 v[236:239], v[102:105], v[142:145], v[236:239]
	v_mfma_f32_16x16x32_f16 v[62:65], v[106:109], v[134:137], v[62:65]
	v_mfma_f32_16x16x32_f16 v[38:41], v[106:109], v[138:141], v[38:41]
	v_mfma_f32_16x16x32_f16 v[34:37], v[106:109], v[142:145], v[34:37]
	s_waitcnt vmcnt(3) lgkmcnt(0)
	s_barrier
	ds_read_b128 v[134:137], v162
	v_mfma_f32_16x16x32_f16 v[82:85], v[110:113], v[146:149], v[82:85]
	ds_read_b128 v[138:141], v162 offset:2048
	v_mfma_f32_16x16x32_f16 v[58:61], v[110:113], v[150:153], v[58:61]
	ds_read_b128 v[142:145], v162 offset:4096
	v_mfma_f32_16x16x32_f16 v[14:17], v[110:113], v[154:157], v[14:17]
	ds_read_b128 v[86:89], v158
	v_mfma_f32_16x16x32_f16 v[78:81], v[114:117], v[146:149], v[78:81]
	ds_read_b128 v[90:93], v158 offset:2048
	v_mfma_f32_16x16x32_f16 v[22:25], v[114:117], v[150:153], v[22:25]
	ds_read_b128 v[94:97], v158 offset:4096
	v_mfma_f32_16x16x32_f16 v[30:33], v[114:117], v[154:157], v[30:33]
	ds_read_b128 v[98:101], v158 offset:6144
	v_mfma_f32_16x16x32_f16 v[74:77], v[118:121], v[146:149], v[74:77]
	ds_read_b128 v[102:105], v158 offset:8192
	v_mfma_f32_16x16x32_f16 v[18:21], v[118:121], v[150:153], v[18:21]
	ds_read_b128 v[106:109], v158 offset:10240
	v_mfma_f32_16x16x32_f16 v[26:29], v[118:121], v[154:157], v[26:29]
	v_mfma_f32_16x16x32_f16 v[70:73], v[122:125], v[146:149], v[70:73]
	v_mfma_f32_16x16x32_f16 v[46:49], v[122:125], v[150:153], v[46:49]
	v_mfma_f32_16x16x32_f16 v[240:243], v[122:125], v[154:157], v[240:243]
	v_mfma_f32_16x16x32_f16 v[66:69], v[126:129], v[146:149], v[66:69]
	v_mfma_f32_16x16x32_f16 v[42:45], v[126:129], v[150:153], v[42:45]
	v_mfma_f32_16x16x32_f16 v[236:239], v[126:129], v[154:157], v[236:239]
	v_mfma_f32_16x16x32_f16 v[62:65], v[130:133], v[146:149], v[62:65]
	v_mfma_f32_16x16x32_f16 v[38:41], v[130:133], v[150:153], v[38:41]
	v_mfma_f32_16x16x32_f16 v[34:37], v[130:133], v[154:157], v[34:37]
	s_waitcnt lgkmcnt(0)
	ds_read_b128 v[146:149], v164
	v_mfma_f32_16x16x32_f16 v[82:85], v[86:89], v[134:137], v[82:85]
	ds_read_b128 v[150:153], v164 offset:2048
	v_mfma_f32_16x16x32_f16 v[58:61], v[86:89], v[138:141], v[58:61]
	ds_read_b128 v[154:157], v164 offset:4096
	v_mfma_f32_16x16x32_f16 v[14:17], v[86:89], v[142:145], v[14:17]
	ds_read_b128 v[110:113], v160
	v_mfma_f32_16x16x32_f16 v[78:81], v[90:93], v[134:137], v[78:81]
	ds_read_b128 v[114:117], v160 offset:2048
	v_mfma_f32_16x16x32_f16 v[22:25], v[90:93], v[138:141], v[22:25]
	ds_read_b128 v[118:121], v160 offset:4096
	v_mfma_f32_16x16x32_f16 v[30:33], v[90:93], v[142:145], v[30:33]
	ds_read_b128 v[122:125], v160 offset:6144
	v_mfma_f32_16x16x32_f16 v[74:77], v[94:97], v[134:137], v[74:77]
	ds_read_b128 v[126:129], v160 offset:8192
	v_mfma_f32_16x16x32_f16 v[18:21], v[94:97], v[138:141], v[18:21]
	ds_read_b128 v[130:133], v160 offset:10240
	v_mfma_f32_16x16x32_f16 v[26:29], v[94:97], v[142:145], v[26:29]
	v_mfma_f32_16x16x32_f16 v[70:73], v[98:101], v[134:137], v[70:73]
	v_mfma_f32_16x16x32_f16 v[46:49], v[98:101], v[138:141], v[46:49]
	v_mfma_f32_16x16x32_f16 v[240:243], v[98:101], v[142:145], v[240:243]
	v_mfma_f32_16x16x32_f16 v[66:69], v[102:105], v[134:137], v[66:69]
	v_mfma_f32_16x16x32_f16 v[42:45], v[102:105], v[138:141], v[42:45]
	v_mfma_f32_16x16x32_f16 v[236:239], v[102:105], v[142:145], v[236:239]
	v_mfma_f32_16x16x32_f16 v[62:65], v[106:109], v[134:137], v[62:65]
	v_mfma_f32_16x16x32_f16 v[38:41], v[106:109], v[138:141], v[38:41]
	v_mfma_f32_16x16x32_f16 v[34:37], v[106:109], v[142:145], v[34:37]
	s_waitcnt lgkmcnt(0)
	v_mfma_f32_16x16x32_f16 v[82:85], v[110:113], v[146:149], v[82:85]
	v_mfma_f32_16x16x32_f16 v[58:61], v[110:113], v[150:153], v[58:61]
	v_mfma_f32_16x16x32_f16 v[14:17], v[110:113], v[154:157], v[14:17]
	v_mfma_f32_16x16x32_f16 v[78:81], v[114:117], v[146:149], v[78:81]
	v_mfma_f32_16x16x32_f16 v[22:25], v[114:117], v[150:153], v[22:25]
	v_mfma_f32_16x16x32_f16 v[30:33], v[114:117], v[154:157], v[30:33]
	v_mfma_f32_16x16x32_f16 v[74:77], v[118:121], v[146:149], v[74:77]
	v_mfma_f32_16x16x32_f16 v[18:21], v[118:121], v[150:153], v[18:21]
	v_mfma_f32_16x16x32_f16 v[26:29], v[118:121], v[154:157], v[26:29]
	v_mfma_f32_16x16x32_f16 v[70:73], v[122:125], v[146:149], v[70:73]
	v_mfma_f32_16x16x32_f16 v[46:49], v[122:125], v[150:153], v[46:49]
	v_mfma_f32_16x16x32_f16 v[240:243], v[122:125], v[154:157], v[240:243]
	v_mfma_f32_16x16x32_f16 v[66:69], v[126:129], v[146:149], v[66:69]
	v_mfma_f32_16x16x32_f16 v[42:45], v[126:129], v[150:153], v[42:45]
	v_mfma_f32_16x16x32_f16 v[236:239], v[126:129], v[154:157], v[236:239]
	v_mfma_f32_16x16x32_f16 v[62:65], v[130:133], v[146:149], v[62:65]
	v_mfma_f32_16x16x32_f16 v[38:41], v[130:133], v[150:153], v[38:41]
	v_mfma_f32_16x16x32_f16 v[34:37], v[130:133], v[154:157], v[34:37]
